# conversion store address: fixed per-lane offset kept in a register for the whole slice run (one 64-bit add per iteration instead of a 64-bit mad + four adds)
# speedup vs baseline: 1.0049x; 1.0049x over previous
; DEVI f32x4 ld_nt(const float* p) { return __builtin_nontemporal_load((const f32x4*)p); }
; DEVI void cv_next(const Params& p, int l, int s, int lane, int stride, CvRun& run) {
;     ...
;     run.c = cv_slice(p, l, s, lane); run.left = 0;
;     if ((stride & 511) == 0) {
;         if (s < NS_W13) { const int e = s >> 9, es = stride >> 9; if (e < NE) { run.left = (NE - 1 - e) / es; run.sstep = (long)es * 1024 * 256; run.dstep = (long)es * 512 * 1024; } }
;         else { const int e = (s - NS_W13) >> 8, es = stride >> 8; if (e < NE) { run.left = (NE - 1 - e) / es; run.sstep = (long)es * 256 * 1024; run.dstep = (long)es * 1024 * 256; } } }
; }
; DEVI void cv_issue(const Params& p, int l, int s, int lane, CvRegs& R, CvRun& run) {
;     R.live = s < NS_SLICES ? 1 : 0;
;     if (R.live) { cv_next(p, l, s, lane, (int)gridDim.x * 8, run); R.c = run.c; const int kq = lane >> 3;
;         const float* sp = R.c.src + (size_t)(R.c.k0 + 2 * kq) * R.c.ld;
;         R.a0 = ld_nt(sp); R.b0 = ld_nt(sp + R.c.ld); R.a1 = ld_nt(sp + (size_t)16 * R.c.ld); R.b1 = ld_nt(sp + (size_t)17 * R.c.ld); }
; DEVI void cv_finish(char* img  , int lane, const CvRegs& R) {
;     ...
;     const int row = R.c.perm ? R.c.r0 + 128 * ((n >> 3) & 1) + 16 * ((n >> 2) & 1) + 4 * (n >> 4) + (n & 3) : R.c.r0 + 128 * ((n >> 2) & 1) + 4 * (n >> 3) + (n & 3);
;     bf16_t* d = R.c.dst + (size_t)row * R.c.K + R.c.k0 + half * 16;
.LBB0_695:
	v_add_u32_e32 v252, s10, v128
	s_mov_b64 s[68:69], s[18:19]
	v_mul_lo_u32 v243, v252, s6
	v_lshlrev_b32_e32 v242, 2, v114
	s_lshl_b32 s72, s6, 2
	s_lshl_b32 s73, s6, 6
	v_lshl_add_u32 v242, v243, 2, v242
	v_add_u32_e32 v243, s72, v242
	v_add_u32_e32 v244, s73, v242
	v_add_u32_e32 v245, s73, v243
	s_cmp_eq_u32 s95, 0
	s_cselect_b64 s[72:73], -1, 0
	v_cndmask_b32_e64 v246, v196, v197, s[72:73]
	v_or_b32_e32 v246, v246, v195
	v_add_u32_e32 v246, s8, v246
	v_mul_lo_u32 v246, v246, s94
	v_add3_u32 v246, v246, v180, s10
	v_lshlrev_b32_e32 v246, 1, v246
	v_mov_b32_e32 v247, 0
	s_ashr_i32 s7, s6, 31
	v_mad_i64_i32 v[252:253], s[16:17], v252, s6, 0
	v_lshl_add_u64 v[252:253], v[252:253], 2, v[250:251]
	s_lshl_b64 s[16:17], s[6:7], 2
	v_lshl_add_u64 v[254:255], v[252:253], 0, s[16:17]
	global_load_dwordx4 v[154:157], v[252:253], off nt
	global_load_dwordx4 v[158:161], v[254:255], off nt
	v_mad_i64_i32 v[252:253], s[18:19], s6, 60, v[254:255]
	v_lshl_add_u64 v[254:255], v[252:253], 0, s[16:17]
	global_load_dwordx4 v[162:165], v[252:253], off nt
	global_load_dwordx4 v[166:169], v[254:255], off nt
	s_mov_b64 s[26:27], s[22:23]
	s_mov_b64 s[28:29], s[50:51]
	s_mov_b32 s56, s11
	s_mov_b32 s55, s95
	v_mov_b64_e32 v[170:171], v[250:251]
	s_mov_b32 s57, s6
	s_mov_b32 s58, s10
	v_mov_b64_e32 v[172:173], v[182:183]
	s_mov_b32 s59, s94
	s_mov_b32 s60, s8

; DEVI unsigned cvt_pk_bf16(float lo, float hi) { unsigned r; asm volatile("v_cvt_pk_bf16_f32 %0, %1, %2" : "=v"(r) : "v"(lo), "v"(hi)); return r; }
; DEVI void cv_finish(char* img  , int lane, const CvRegs& R) {
;     if (!R.live) return;
;     const int n4 = (lane & 7) * 4, kq = lane >> 3;
;     const float sc = R.c.perm ? 16.f : 1.f;
; #pragma unroll
;     for (int c = 0; c < 4; ++c) { *(unsigned*)(img + (n4 + c) * 68 + (2 * kq) * 2) = cvt_pk_bf16(R.a0[c] * sc, R.b0[c] * sc); *(unsigned*)(img + (n4 + c) * 68 + (2 * kq + 16) * 2) = cvt_pk_bf16(R.a1[c] * sc, R.b1[c] * sc); }
;     asm volatile("" ::: "memory"); __builtin_amdgcn_wave_barrier();
.LBB0_710:
	s_cmp_eq_u32 s95, 0
	s_cselect_b64 vcc, -1, 0
	s_waitcnt vmcnt(0)
	s_cbranch_scc0 .Lmy_cvs_a
	v_add_u32_e32 v68, v200, v201
	v_cvt_pk_bf16_f32 v67, v154, v158
	v_cvt_pk_bf16_f32 v69, v162, v166
	ds_write2_b32 v68, v67, v69 offset0:0 offset1:8
	v_cvt_pk_bf16_f32 v67, v155, v159
	v_cvt_pk_bf16_f32 v69, v163, v167
	ds_write2_b32 v68, v67, v69 offset0:17 offset1:25
	v_cvt_pk_bf16_f32 v67, v156, v160
	v_cvt_pk_bf16_f32 v69, v164, v168
	ds_write2_b32 v68, v67, v69 offset0:34 offset1:42
	v_cvt_pk_bf16_f32 v67, v157, v161
	v_cvt_pk_bf16_f32 v69, v165, v169
	ds_write2_b32 v68, v67, v69 offset0:51 offset1:59
	v_add_u32_e32 v68, v198, v199

; DEVI unsigned cvt_pk_bf16(float lo, float hi) { unsigned r; asm volatile("v_cvt_pk_bf16_f32 %0, %1, %2" : "=v"(r) : "v"(lo), "v"(hi)); return r; }
; DEVI void cv_finish(char* img  , int lane, const CvRegs& R) {
;     if (!R.live) return;
;     const int n4 = (lane & 7) * 4, kq = lane >> 3;
;     const float sc = R.c.perm ? 16.f : 1.f;
; #pragma unroll
;     for (int c = 0; c < 4; ++c) { *(unsigned*)(img + (n4 + c) * 68 + (2 * kq) * 2) = cvt_pk_bf16(R.a0[c] * sc, R.b0[c] * sc); *(unsigned*)(img + (n4 + c) * 68 + (2 * kq + 16) * 2) = cvt_pk_bf16(R.a1[c] * sc, R.b1[c] * sc); }
;     asm volatile("" ::: "memory"); __builtin_amdgcn_wave_barrier();
;     const int n = lane >> 1, half = lane & 1; u32x4 w0, w1;
; #pragma unroll
;     for (int j = 0; j < 4; ++j) { w0[j] = *(const unsigned*)(img + n * 68 + half * 32 + j * 4); w1[j] = *(const unsigned*)(img + n * 68 + half * 32 + 16 + j * 4); }
;     const int row = R.c.perm ? R.c.r0 + 128 * ((n >> 3) & 1) + 16 * ((n >> 2) & 1) + 4 * (n >> 4) + (n & 3) : R.c.r0 + 128 * ((n >> 2) & 1) + 4 * (n >> 3) + (n & 3);
;     bf16_t* d = R.c.dst + (size_t)row * R.c.K + R.c.k0 + half * 16;
	s_branch .Lmy_cvj_a

; DEVI void cv_finish(char* img  , int lane, const CvRegs& R) {
;     ...
;     const int n = lane >> 1, half = lane & 1; u32x4 w0, w1;
; #pragma unroll
;     for (int j = 0; j < 4; ++j) { w0[j] = *(const unsigned*)(img + n * 68 + half * 32 + j * 4); w1[j] = *(const unsigned*)(img + n * 68 + half * 32 + 16 + j * 4); }
;     const int row = R.c.perm ? R.c.r0 + 128 * ((n >> 3) & 1) + 16 * ((n >> 2) & 1) + 4 * (n >> 4) + (n & 3) : R.c.r0 + 128 * ((n >> 2) & 1) + 4 * (n >> 3) + (n & 3);
;     bf16_t* d = R.c.dst + (size_t)row * R.c.K + R.c.k0 + half * 16;
.Lmy_cvj_a:
	ds_read2_b32 v[66:67], v68 offset1:1
	ds_read2_b32 v[70:71], v68 offset0:4 offset1:5
	ds_read2_b32 v[72:73], v68 offset0:6 offset1:7
	ds_read2_b32 v[68:69], v68 offset0:2 offset1:3
	v_lshl_add_u64 v[74:75], v[172:173], 0, v[246:247]


; DEVI void cv_finish(char* img  , int lane, const CvRegs& R) {
;     ...
;     bf16_t* d = R.c.dst + (size_t)row * R.c.K + R.c.k0 + half * 16;
;     __builtin_nontemporal_store(w0, (u32x4*)d); __builtin_nontemporal_store(w1, (u32x4*)(d + 8));
;     asm volatile("" ::: "memory"); __builtin_amdgcn_wave_barrier();
	s_waitcnt lgkmcnt(0)
	global_store_dwordx4 v[74:75], v[66:69], off nt
	global_store_dwordx4 v[74:75], v[70:73], off offset:16 nt
	s_waitcnt vmcnt(2)
	s_cbranch_execz .LBB0_701
	s_branch .LBB0_702

; DEVI f32x4 ld_nt(const float* p) { return __builtin_nontemporal_load((const f32x4*)p); }
; DEVI void cv_next(const Params& p, int l, int s, int lane, int stride, CvRun& run) {
;     ...
;     run.c = cv_slice(p, l, s, lane); run.left = 0;
;     if ((stride & 511) == 0) {
;         if (s < NS_W13) { const int e = s >> 9, es = stride >> 9; if (e < NE) { run.left = (NE - 1 - e) / es; run.sstep = (long)es * 1024 * 256; run.dstep = (long)es * 512 * 1024; } }
;         else { const int e = (s - NS_W13) >> 8, es = stride >> 8; if (e < NE) { run.left = (NE - 1 - e) / es; run.sstep = (long)es * 256 * 1024; run.dstep = (long)es * 1024 * 256; } } }
; }
; DEVI void cv_issue(const Params& p, int l, int s, int lane, CvRegs& R, CvRun& run) {
;     R.live = s < NS_SLICES ? 1 : 0;
;     if (R.live) { cv_next(p, l, s, lane, (int)gridDim.x * 8, run); R.c = run.c; const int kq = lane >> 3;
;         const float* sp = R.c.src + (size_t)(R.c.k0 + 2 * kq) * R.c.ld;
;         R.a0 = ld_nt(sp); R.b0 = ld_nt(sp + R.c.ld); R.a1 = ld_nt(sp + (size_t)16 * R.c.ld); R.b1 = ld_nt(sp + (size_t)17 * R.c.ld); }
; DEVI void cv_finish(char* img  , int lane, const CvRegs& R) {
;     ...
;     const int row = R.c.perm ? R.c.r0 + 128 * ((n >> 3) & 1) + 16 * ((n >> 2) & 1) + 4 * (n >> 4) + (n & 3) : R.c.r0 + 128 * ((n >> 2) & 1) + 4 * (n >> 3) + (n & 3);
;     bf16_t* d = R.c.dst + (size_t)row * R.c.K + R.c.k0 + half * 16;
.LBB0_747:
	v_add_u32_e32 v84, s10, v128
	v_mul_lo_u32 v243, v84, s6
	v_lshlrev_b32_e32 v242, 2, v114
	s_lshl_b32 s72, s6, 2
	s_lshl_b32 s73, s6, 6
	v_lshl_add_u32 v242, v243, 2, v242
	v_add_u32_e32 v243, s72, v242
	v_add_u32_e32 v244, s73, v242
	v_add_u32_e32 v245, s73, v243
	s_cmp_eq_u32 s95, 0
	s_cselect_b64 s[72:73], -1, 0
	v_cndmask_b32_e64 v246, v196, v197, s[72:73]
	v_or_b32_e32 v246, v246, v195
	v_add_u32_e32 v246, s8, v246
	v_mul_lo_u32 v246, v246, s94
	v_add3_u32 v246, v246, v180, s10
	v_lshlrev_b32_e32 v246, 1, v246
	v_mov_b32_e32 v247, 0
	s_ashr_i32 s7, s6, 31
	v_mad_i64_i32 v[84:85], s[14:15], v84, s6, 0
	v_lshl_add_u64 v[84:85], v[84:85], 2, v[82:83]
	s_lshl_b64 s[14:15], s[6:7], 2
	v_lshl_add_u64 v[86:87], v[84:85], 0, s[14:15]
	global_load_dwordx4 v[154:157], v[84:85], off nt
	global_load_dwordx4 v[158:161], v[86:87], off nt
	v_mad_i64_i32 v[84:85], s[16:17], s6, 60, v[86:87]
	v_lshl_add_u64 v[86:87], v[84:85], 0, s[14:15]
	global_load_dwordx4 v[162:165], v[84:85], off nt
	global_load_dwordx4 v[166:169], v[86:87], off nt
	s_mov_b64 s[26:27], s[20:21]
	s_mov_b64 s[28:29], s[22:23]
	s_mov_b32 s56, s2
	s_mov_b32 s55, s95
	v_mov_b64_e32 v[170:171], v[82:83]
	s_mov_b32 s57, s6
	s_mov_b32 s58, s10
	v_mov_b64_e32 v[172:173], v[182:183]
	s_mov_b32 s59, s94
	s_mov_b32 s60, s8

; DEVI f32x4 ld_nt(const float* p) { return __builtin_nontemporal_load((const f32x4*)p); }
; DEVI void cv_next(const Params& p, int l, int s, int lane, int stride, CvRun& run) {
;     ...
;     run.c = cv_slice(p, l, s, lane); run.left = 0;
;     if ((stride & 511) == 0) {
;         if (s < NS_W13) { const int e = s >> 9, es = stride >> 9; if (e < NE) { run.left = (NE - 1 - e) / es; run.sstep = (long)es * 1024 * 256; run.dstep = (long)es * 512 * 1024; } }
;         else { const int e = (s - NS_W13) >> 8, es = stride >> 8; if (e < NE) { run.left = (NE - 1 - e) / es; run.sstep = (long)es * 256 * 1024; run.dstep = (long)es * 1024 * 256; } } }
; }
; DEVI void cv_issue(const Params& p, int l, int s, int lane, CvRegs& R, CvRun& run) {
;     R.live = s < NS_SLICES ? 1 : 0;
;     if (R.live) { cv_next(p, l, s, lane, (int)gridDim.x * 8, run); R.c = run.c; const int kq = lane >> 3;
;         const float* sp = R.c.src + (size_t)(R.c.k0 + 2 * kq) * R.c.ld;
;         R.a0 = ld_nt(sp); R.b0 = ld_nt(sp + R.c.ld); R.a1 = ld_nt(sp + (size_t)16 * R.c.ld); R.b1 = ld_nt(sp + (size_t)17 * R.c.ld); }
; DEVI void cv_finish(char* img  , int lane, const CvRegs& R) {
;     ...
;     const int row = R.c.perm ? R.c.r0 + 128 * ((n >> 3) & 1) + 16 * ((n >> 2) & 1) + 4 * (n >> 4) + (n & 3) : R.c.r0 + 128 * ((n >> 2) & 1) + 4 * (n >> 3) + (n & 3);
;     bf16_t* d = R.c.dst + (size_t)row * R.c.K + R.c.k0 + half * 16;
.LBB0_2259:
	v_add_u32_e32 v252, s10, v128
	s_mov_b64 s[68:69], s[18:19]
	v_mul_lo_u32 v243, v252, s6
	v_lshlrev_b32_e32 v242, 2, v114
	s_lshl_b32 s72, s6, 2
	s_lshl_b32 s73, s6, 6
	v_lshl_add_u32 v242, v243, 2, v242
	v_add_u32_e32 v243, s72, v242
	v_add_u32_e32 v244, s73, v242
	v_add_u32_e32 v245, s73, v243
	s_cmp_eq_u32 s95, 0
	s_cselect_b64 s[72:73], -1, 0
	v_cndmask_b32_e64 v246, v197, v198, s[72:73]
	v_or_b32_e32 v246, v246, v196
	v_add_u32_e32 v246, s8, v246
	v_mul_lo_u32 v246, v246, s94
	v_add3_u32 v246, v246, v180, s10
	v_lshlrev_b32_e32 v246, 1, v246
	v_mov_b32_e32 v247, 0
	s_ashr_i32 s7, s6, 31
	v_mad_i64_i32 v[252:253], s[16:17], v252, s6, 0
	v_lshl_add_u64 v[252:253], v[252:253], 2, v[250:251]
	s_lshl_b64 s[16:17], s[6:7], 2
	v_lshl_add_u64 v[254:255], v[252:253], 0, s[16:17]
	global_load_dwordx4 v[154:157], v[252:253], off nt
	global_load_dwordx4 v[158:161], v[254:255], off nt
	v_mad_i64_i32 v[252:253], s[18:19], s6, 60, v[254:255]
	v_lshl_add_u64 v[254:255], v[252:253], 0, s[16:17]
	global_load_dwordx4 v[162:165], v[252:253], off nt
	global_load_dwordx4 v[166:169], v[254:255], off nt
	s_mov_b64 s[26:27], s[22:23]
	s_mov_b64 s[28:29], s[50:51]
	s_mov_b32 s56, s11
	s_mov_b32 s55, s95
	v_mov_b64_e32 v[170:171], v[250:251]
	s_mov_b32 s57, s6
	s_mov_b32 s58, s10
	v_mov_b64_e32 v[172:173], v[182:183]
	s_mov_b32 s59, s94
	s_mov_b32 s60, s8

; DEVI unsigned cvt_pk_bf16(float lo, float hi) { unsigned r; asm volatile("v_cvt_pk_bf16_f32 %0, %1, %2" : "=v"(r) : "v"(lo), "v"(hi)); return r; }
; DEVI void cv_finish(char* img  , int lane, const CvRegs& R) {
;     if (!R.live) return;
;     const int n4 = (lane & 7) * 4, kq = lane >> 3;
;     const float sc = R.c.perm ? 16.f : 1.f;
; #pragma unroll
;     for (int c = 0; c < 4; ++c) { *(unsigned*)(img + (n4 + c) * 68 + (2 * kq) * 2) = cvt_pk_bf16(R.a0[c] * sc, R.b0[c] * sc); *(unsigned*)(img + (n4 + c) * 68 + (2 * kq + 16) * 2) = cvt_pk_bf16(R.a1[c] * sc, R.b1[c] * sc); }
;     asm volatile("" ::: "memory"); __builtin_amdgcn_wave_barrier();
.LBB0_2274:
	s_cmp_eq_u32 s95, 0
	s_cselect_b64 vcc, -1, 0
	s_waitcnt vmcnt(0)
	s_cbranch_scc0 .Lmy_cvs_b
	v_add_u32_e32 v68, v201, v202
	v_cvt_pk_bf16_f32 v67, v154, v158
	v_cvt_pk_bf16_f32 v69, v162, v166
	ds_write2_b32 v68, v67, v69 offset0:0 offset1:8
	v_cvt_pk_bf16_f32 v67, v155, v159
	v_cvt_pk_bf16_f32 v69, v163, v167
	ds_write2_b32 v68, v67, v69 offset0:17 offset1:25
	v_cvt_pk_bf16_f32 v67, v156, v160
	v_cvt_pk_bf16_f32 v69, v164, v168
	ds_write2_b32 v68, v67, v69 offset0:34 offset1:42
	v_cvt_pk_bf16_f32 v67, v157, v161
	v_cvt_pk_bf16_f32 v69, v165, v169
	ds_write2_b32 v68, v67, v69 offset0:51 offset1:59
	v_add_u32_e32 v68, v199, v200

; DEVI unsigned cvt_pk_bf16(float lo, float hi) { unsigned r; asm volatile("v_cvt_pk_bf16_f32 %0, %1, %2" : "=v"(r) : "v"(lo), "v"(hi)); return r; }
; DEVI void cv_finish(char* img  , int lane, const CvRegs& R) {
;     if (!R.live) return;
;     const int n4 = (lane & 7) * 4, kq = lane >> 3;
;     const float sc = R.c.perm ? 16.f : 1.f;
; #pragma unroll
;     for (int c = 0; c < 4; ++c) { *(unsigned*)(img + (n4 + c) * 68 + (2 * kq) * 2) = cvt_pk_bf16(R.a0[c] * sc, R.b0[c] * sc); *(unsigned*)(img + (n4 + c) * 68 + (2 * kq + 16) * 2) = cvt_pk_bf16(R.a1[c] * sc, R.b1[c] * sc); }
;     asm volatile("" ::: "memory"); __builtin_amdgcn_wave_barrier();
;     const int n = lane >> 1, half = lane & 1; u32x4 w0, w1;
; #pragma unroll
;     for (int j = 0; j < 4; ++j) { w0[j] = *(const unsigned*)(img + n * 68 + half * 32 + j * 4); w1[j] = *(const unsigned*)(img + n * 68 + half * 32 + 16 + j * 4); }
;     const int row = R.c.perm ? R.c.r0 + 128 * ((n >> 3) & 1) + 16 * ((n >> 2) & 1) + 4 * (n >> 4) + (n & 3) : R.c.r0 + 128 * ((n >> 2) & 1) + 4 * (n >> 3) + (n & 3);
;     bf16_t* d = R.c.dst + (size_t)row * R.c.K + R.c.k0 + half * 16;
	s_branch .Lmy_cvj_b

; DEVI f32x4 ld_nt(const float* p) { return __builtin_nontemporal_load((const f32x4*)p); }
; DEVI void cv_next(const Params& p, int l, int s, int lane, int stride, CvRun& run) {
;     ...
;     run.c = cv_slice(p, l, s, lane); run.left = 0;
;     if ((stride & 511) == 0) {
;         if (s < NS_W13) { const int e = s >> 9, es = stride >> 9; if (e < NE) { run.left = (NE - 1 - e) / es; run.sstep = (long)es * 1024 * 256; run.dstep = (long)es * 512 * 1024; } }
;         else { const int e = (s - NS_W13) >> 8, es = stride >> 8; if (e < NE) { run.left = (NE - 1 - e) / es; run.sstep = (long)es * 256 * 1024; run.dstep = (long)es * 1024 * 256; } } }
; }
; DEVI void cv_issue(const Params& p, int l, int s, int lane, CvRegs& R, CvRun& run) {
;     R.live = s < NS_SLICES ? 1 : 0;
;     if (R.live) { cv_next(p, l, s, lane, (int)gridDim.x * 8, run); R.c = run.c; const int kq = lane >> 3;
;         const float* sp = R.c.src + (size_t)(R.c.k0 + 2 * kq) * R.c.ld;
;         R.a0 = ld_nt(sp); R.b0 = ld_nt(sp + R.c.ld); R.a1 = ld_nt(sp + (size_t)16 * R.c.ld); R.b1 = ld_nt(sp + (size_t)17 * R.c.ld); }
; DEVI void cv_finish(char* img  , int lane, const CvRegs& R) {
;     ...
;     const int row = R.c.perm ? R.c.r0 + 128 * ((n >> 3) & 1) + 16 * ((n >> 2) & 1) + 4 * (n >> 4) + (n & 3) : R.c.r0 + 128 * ((n >> 2) & 1) + 4 * (n >> 3) + (n & 3);
;     bf16_t* d = R.c.dst + (size_t)row * R.c.K + R.c.k0 + half * 16;
.LBB0_2311:
	v_add_u32_e32 v84, s10, v128
	v_mul_lo_u32 v243, v84, s6
	v_lshlrev_b32_e32 v242, 2, v114
	s_lshl_b32 s72, s6, 2
	s_lshl_b32 s73, s6, 6
	v_lshl_add_u32 v242, v243, 2, v242
	v_add_u32_e32 v243, s72, v242
	v_add_u32_e32 v244, s73, v242
	v_add_u32_e32 v245, s73, v243
	s_cmp_eq_u32 s95, 0
	s_cselect_b64 s[72:73], -1, 0
	v_cndmask_b32_e64 v246, v197, v198, s[72:73]
	v_or_b32_e32 v246, v246, v196
	v_add_u32_e32 v246, s8, v246
	v_mul_lo_u32 v246, v246, s94
	v_add3_u32 v246, v246, v180, s10
	v_lshlrev_b32_e32 v246, 1, v246
	v_mov_b32_e32 v247, 0
	s_ashr_i32 s7, s6, 31
	v_mad_i64_i32 v[84:85], s[14:15], v84, s6, 0
	v_lshl_add_u64 v[84:85], v[84:85], 2, v[82:83]
	s_lshl_b64 s[14:15], s[6:7], 2
	v_lshl_add_u64 v[86:87], v[84:85], 0, s[14:15]
	global_load_dwordx4 v[154:157], v[84:85], off nt
	global_load_dwordx4 v[158:161], v[86:87], off nt
	v_mad_i64_i32 v[84:85], s[16:17], s6, 60, v[86:87]
	v_lshl_add_u64 v[86:87], v[84:85], 0, s[14:15]
	global_load_dwordx4 v[162:165], v[84:85], off nt
	global_load_dwordx4 v[166:169], v[86:87], off nt
	s_mov_b64 s[26:27], s[20:21]
	s_mov_b64 s[28:29], s[22:23]
	s_mov_b32 s56, s2
	s_mov_b32 s55, s95
	v_mov_b64_e32 v[170:171], v[82:83]
	s_mov_b32 s57, s6
	s_mov_b32 s58, s10
	v_mov_b64_e32 v[172:173], v[182:183]
	s_mov_b32 s59, s94
	s_mov_b32 s60, s8
